# speedup vs baseline: 1.0239x; 1.0014x over previous
.LBB1_1:
	s_barrier
	s_add_i32 s42, s35, s94
	s_and_b32 s97, s42, 15
	s_lshl_b32 s98, s97, 3
	s_add_i32 s42, s42, 1
	s_and_b32 s99, s42, 15
	s_lshl_b32 s42, s99, 16
	s_add_i32 s42, s95, s42
	s_or_b32 s43, s42, 0x400
	buffer_load_dwordx4 v[146:149], v195, s[44:47], s42 offen
	buffer_load_dwordx4 v[150:153], v195, s[44:47], s43 offen
	s_or_b32 s43, s42, 0x800
	s_or_b32 s48, s42, 0xc00
	buffer_load_dwordx4 v[138:141], v195, s[44:47], s43 offen
	buffer_load_dwordx4 v[142:145], v195, s[44:47], s48 offen
	s_or_b32 s43, s42, 0x1000
	s_or_b32 s48, s42, 0x1400
	buffer_load_dwordx4 v[122:125], v195, s[44:47], s43 offen
	buffer_load_dwordx4 v[126:129], v195, s[44:47], s48 offen
	s_or_b32 s43, s42, 0x1800
	s_or_b32 s42, s42, 0x1c00
	buffer_load_dwordx4 v[130:133], v195, s[44:47], s43 offen
	buffer_load_dwordx4 v[134:137], v195, s[44:47], s42 offen
	s_add_i32 s98, s98, s52
	s_cmp_lg_u32 s98, s33
	s_cbranch_scc1 .LBB1_3
	v_cndmask_b32_e64 v2, v2, v198, s[0:1]
	v_cndmask_b32_e64 v3, v3, v198, s[2:3]
	v_cndmask_b32_e64 v4, v4, v198, s[4:5]
	v_cndmask_b32_e64 v5, v5, v198, s[6:7]
	v_cndmask_b32_e64 v6, v6, v198, s[8:9]
	v_cndmask_b32_e64 v7, v7, v198, s[10:11]
	v_cndmask_b32_e64 v8, v8, v198, s[12:13]
	v_cndmask_b32_e64 v9, v9, v198, s[14:15]
	v_cndmask_b32_e64 v10, v10, v198, s[16:17]
	v_cndmask_b32_e64 v11, v11, v198, s[18:19]
	v_cndmask_b32_e64 v12, v12, v198, s[20:21]
	v_cndmask_b32_e64 v13, v13, v198, s[22:23]
	v_cndmask_b32_e64 v14, v14, v198, s[24:25]
	v_cndmask_b32_e64 v15, v15, v198, s[26:27]
	v_cndmask_b32_e64 v16, v16, v198, s[28:29]
	v_cndmask_b32_e64 v17, v17, v198, s[30:31]
